# baseline (speedup 1.0000x reference)
.LBB1_10:
	s_andn2_b32 s38, 1, s33
	s_lshl_b32 s39, s38, 4
	s_add_i32 s39, s39, s27
	s_add_i32 s39, s39, 0x20800
	v_mov_b32_e32 v213, s39
	ds_read_b64 v[214:215], v213
	v_add_u32_e32 v238, s31, v200
	ds_read_b64_tr_b16 v[222:223], v238 offset:0
	v_add_u32_e32 v239, s31, v201
	ds_read_b64_tr_b16 v[224:225], v239 offset:0
	v_add_u32_e32 v240, s31, v202
	ds_read_b64_tr_b16 v[226:227], v240 offset:0
	v_add_u32_e32 v241, s31, v203
	ds_read_b64_tr_b16 v[228:229], v241 offset:0
	v_add_u32_e32 v242, s31, v204
	ds_read_b64_tr_b16 v[230:231], v242 offset:0
	v_add_u32_e32 v243, s31, v205
	ds_read_b64_tr_b16 v[232:233], v243 offset:0
	v_add_u32_e32 v244, s31, v206
	ds_read_b64_tr_b16 v[234:235], v244 offset:0
	v_add_u32_e32 v245, s31, v207
	ds_read_b64_tr_b16 v[236:237], v245 offset:0
	s_add_i32 s29, s28, 0x8000
	s_cmp_lg_u32 s28, 0x10000
	s_cselect_b32 s29, s29, 0
	s_add_i32 s36, s19, s29
	s_mov_b32 m0, s36
	s_nop 0
	global_load_lds_dwordx4 v199, s[16:17]
	s_add_i32 s34, s36, 0x400
	s_mov_b32 m0, s34
	s_nop 0
	global_load_lds_dwordx4 v208, s[16:17]
	s_add_u32 s34, s16, 0x2000
	s_addc_u32 s35, s17, 0
	s_add_i32 s37, s36, 0x2000
	s_mov_b32 m0, s37
	s_nop 0
	global_load_lds_dwordx4 v199, s[34:35]
	s_add_i32 s37, s36, 0x2400
	s_mov_b32 m0, s37
	s_nop 0
	global_load_lds_dwordx4 v208, s[34:35]
	s_add_u32 s34, s16, 0x4000
	s_addc_u32 s35, s17, 0
	s_add_i32 s37, s36, 0x4000
	s_mov_b32 m0, s37
	s_nop 0
	global_load_lds_dwordx4 v199, s[34:35]
	s_add_i32 s37, s36, 0x4400
	s_mov_b32 m0, s37
	s_nop 0
	global_load_lds_dwordx4 v208, s[34:35]
	s_add_u32 s16, s16, 0x6000
	s_addc_u32 s17, s17, 0
	s_add_i32 s34, s36, 0x6000
	s_mov_b32 m0, s34
	s_nop 0
	global_load_lds_dwordx4 v199, s[16:17]
	s_addk_i32 s36, 0x6400
	s_mov_b32 m0, s36
	s_nop 0
	global_load_lds_dwordx4 v208, s[16:17]
	s_andn2_b32 s16, 1, s33
	s_waitcnt lgkmcnt(8)
	v_readfirstlane_b32 s17, v214
	s_cmp_eq_u32 s33, 1
	s_cbranch_scc1 .LBB1_14
	s_cmp_eq_u32 s17, 0
	v_readfirstlane_b32 s17, v215
	s_cbranch_scc1 .LBB1_12
	v_lshl_add_u32 v213, s16, 10, v210
	ds_read_b32 v214, v213
	s_waitcnt lgkmcnt(0)
	v_pk_mul_f32 v[126:127], v[214:215], v[126:127] op_sel_hi:[0,1]
	v_pk_mul_f32 v[124:125], v[214:215], v[124:125] op_sel_hi:[0,1]
	v_pk_mul_f32 v[122:123], v[214:215], v[122:123] op_sel_hi:[0,1]
	v_pk_mul_f32 v[120:121], v[214:215], v[120:121] op_sel_hi:[0,1]
	v_pk_mul_f32 v[118:119], v[214:215], v[118:119] op_sel_hi:[0,1]
	v_pk_mul_f32 v[116:117], v[214:215], v[116:117] op_sel_hi:[0,1]
	v_pk_mul_f32 v[114:115], v[214:215], v[114:115] op_sel_hi:[0,1]
	v_pk_mul_f32 v[112:113], v[214:215], v[112:113] op_sel_hi:[0,1]
	v_pk_mul_f32 v[94:95], v[214:215], v[94:95] op_sel_hi:[0,1]
	v_pk_mul_f32 v[92:93], v[214:215], v[92:93] op_sel_hi:[0,1]
	v_pk_mul_f32 v[90:91], v[214:215], v[90:91] op_sel_hi:[0,1]
	v_pk_mul_f32 v[88:89], v[214:215], v[88:89] op_sel_hi:[0,1]
	v_pk_mul_f32 v[86:87], v[214:215], v[86:87] op_sel_hi:[0,1]
	v_pk_mul_f32 v[84:85], v[214:215], v[84:85] op_sel_hi:[0,1]
	v_pk_mul_f32 v[82:83], v[214:215], v[82:83] op_sel_hi:[0,1]
	v_pk_mul_f32 v[80:81], v[214:215], v[80:81] op_sel_hi:[0,1]
	v_pk_mul_f32 v[62:63], v[214:215], v[62:63] op_sel_hi:[0,1]
	v_pk_mul_f32 v[60:61], v[214:215], v[60:61] op_sel_hi:[0,1]
	v_pk_mul_f32 v[58:59], v[214:215], v[58:59] op_sel_hi:[0,1]
	v_pk_mul_f32 v[56:57], v[214:215], v[56:57] op_sel_hi:[0,1]
	v_pk_mul_f32 v[54:55], v[214:215], v[54:55] op_sel_hi:[0,1]
	v_pk_mul_f32 v[52:53], v[214:215], v[52:53] op_sel_hi:[0,1]
	v_pk_mul_f32 v[50:51], v[214:215], v[50:51] op_sel_hi:[0,1]
	v_pk_mul_f32 v[48:49], v[214:215], v[48:49] op_sel_hi:[0,1]
	v_pk_mul_f32 v[14:15], v[214:215], v[14:15] op_sel_hi:[0,1]
	v_pk_mul_f32 v[12:13], v[214:215], v[12:13] op_sel_hi:[0,1]
	v_pk_mul_f32 v[10:11], v[214:215], v[10:11] op_sel_hi:[0,1]
	v_pk_mul_f32 v[8:9], v[214:215], v[8:9] op_sel_hi:[0,1]
	v_pk_mul_f32 v[6:7], v[214:215], v[6:7] op_sel_hi:[0,1]
	v_pk_mul_f32 v[4:5], v[214:215], v[4:5] op_sel_hi:[0,1]
	v_pk_mul_f32 v[2:3], v[214:215], v[2:3] op_sel_hi:[0,1]
	v_pk_mul_f32 v[0:1], v[214:215], v[0:1] op_sel_hi:[0,1]

.LBB1_14:
	v_lshl_add_u32 v213, s16, 14, v212
	ds_read_b128 v[214:217], v213 offset:0
	ds_read_b128 v[218:221], v213 offset:0x1000
	s_add_u32 s6, s6, 0x8000
	s_waitcnt lgkmcnt(0)
	s_addc_u32 s7, s7, 0
	v_mfma_f32_32x32x16_bf16 v[112:127], v[222:225], v[214:217], v[112:127]
	s_cmp_eq_u32 s30, 17
	v_mfma_f32_32x32x16_bf16 v[96:111], v[222:225], v[218:221], v[96:111]
	v_mfma_f32_32x32x16_bf16 v[80:95], v[226:229], v[214:217], v[80:95]
	v_mfma_f32_32x32x16_bf16 v[64:79], v[226:229], v[218:221], v[64:79]
	v_mfma_f32_32x32x16_bf16 v[48:63], v[230:233], v[214:217], v[48:63]
	v_mfma_f32_32x32x16_bf16 v[32:47], v[230:233], v[218:221], v[32:47]
	v_mfma_f32_32x32x16_bf16 v[0:15], v[234:237], v[214:217], v[0:15]
	ds_read_b128 v[214:217], v213 offset:0x400
	v_mfma_f32_32x32x16_bf16 v[16:31], v[234:237], v[218:221], v[16:31]
	ds_read_b128 v[218:221], v213 offset:0x1400
	ds_read_b64_tr_b16 v[222:223], v238 offset:0x2000
	ds_read_b64_tr_b16 v[224:225], v239 offset:0x2000
	ds_read_b64_tr_b16 v[226:227], v240 offset:0x2000
	ds_read_b64_tr_b16 v[228:229], v241 offset:0x2000
	ds_read_b64_tr_b16 v[230:231], v242 offset:0x2000
	ds_read_b64_tr_b16 v[232:233], v243 offset:0x2000
	ds_read_b64_tr_b16 v[234:235], v244 offset:0x2000
	ds_read_b64_tr_b16 v[236:237], v245 offset:0x2000
	s_nop 0
	s_waitcnt lgkmcnt(0)
	s_nop 0
	v_mfma_f32_32x32x16_bf16 v[112:127], v[222:225], v[214:217], v[112:127]
	v_mfma_f32_32x32x16_bf16 v[96:111], v[222:225], v[218:221], v[96:111]
	v_mfma_f32_32x32x16_bf16 v[80:95], v[226:229], v[214:217], v[80:95]
	v_mfma_f32_32x32x16_bf16 v[64:79], v[226:229], v[218:221], v[64:79]
	v_mfma_f32_32x32x16_bf16 v[48:63], v[230:233], v[214:217], v[48:63]
	v_mfma_f32_32x32x16_bf16 v[32:47], v[230:233], v[218:221], v[32:47]
	v_mfma_f32_32x32x16_bf16 v[0:15], v[234:237], v[214:217], v[0:15]
	ds_read_b128 v[214:217], v213 offset:0x800
	v_mfma_f32_32x32x16_bf16 v[16:31], v[234:237], v[218:221], v[16:31]
	ds_read_b128 v[218:221], v213 offset:0x1800
	ds_read_b64_tr_b16 v[222:223], v238 offset:0x4000
	ds_read_b64_tr_b16 v[224:225], v239 offset:0x4000
	ds_read_b64_tr_b16 v[226:227], v240 offset:0x4000
	ds_read_b64_tr_b16 v[228:229], v241 offset:0x4000
	ds_read_b64_tr_b16 v[230:231], v242 offset:0x4000
	ds_read_b64_tr_b16 v[232:233], v243 offset:0x4000
	ds_read_b64_tr_b16 v[234:235], v244 offset:0x4000
	ds_read_b64_tr_b16 v[236:237], v245 offset:0x4000
	s_nop 0
	s_waitcnt lgkmcnt(0)
	s_nop 0
	v_mfma_f32_32x32x16_bf16 v[112:127], v[222:225], v[214:217], v[112:127]
	v_mfma_f32_32x32x16_bf16 v[96:111], v[222:225], v[218:221], v[96:111]
	v_mfma_f32_32x32x16_bf16 v[80:95], v[226:229], v[214:217], v[80:95]
	v_mfma_f32_32x32x16_bf16 v[64:79], v[226:229], v[218:221], v[64:79]
	v_mfma_f32_32x32x16_bf16 v[48:63], v[230:233], v[214:217], v[48:63]
	v_mfma_f32_32x32x16_bf16 v[32:47], v[230:233], v[218:221], v[32:47]
	v_mfma_f32_32x32x16_bf16 v[0:15], v[234:237], v[214:217], v[0:15]
	ds_read_b128 v[214:217], v213 offset:0xc00
	v_mfma_f32_32x32x16_bf16 v[16:31], v[234:237], v[218:221], v[16:31]
	ds_read_b128 v[218:221], v213 offset:0x1c00
	ds_read_b64_tr_b16 v[222:223], v238 offset:0x6000
	ds_read_b64_tr_b16 v[224:225], v239 offset:0x6000
	ds_read_b64_tr_b16 v[226:227], v240 offset:0x6000
	ds_read_b64_tr_b16 v[228:229], v241 offset:0x6000
	ds_read_b64_tr_b16 v[230:231], v242 offset:0x6000
	ds_read_b64_tr_b16 v[232:233], v243 offset:0x6000
	ds_read_b64_tr_b16 v[234:235], v244 offset:0x6000
	ds_read_b64_tr_b16 v[236:237], v245 offset:0x6000
	s_nop 0
	s_waitcnt lgkmcnt(0)
	s_waitcnt vmcnt(0)
	s_nop 0
	v_mfma_f32_32x32x16_bf16 v[112:127], v[222:225], v[214:217], v[112:127]
	s_barrier
	v_mfma_f32_32x32x16_bf16 v[96:111], v[222:225], v[218:221], v[96:111]
	v_mfma_f32_32x32x16_bf16 v[80:95], v[226:229], v[214:217], v[80:95]
	v_mfma_f32_32x32x16_bf16 v[64:79], v[226:229], v[218:221], v[64:79]
	v_mfma_f32_32x32x16_bf16 v[48:63], v[230:233], v[214:217], v[48:63]
	v_mfma_f32_32x32x16_bf16 v[32:47], v[230:233], v[218:221], v[32:47]
	v_mfma_f32_32x32x16_bf16 v[0:15], v[234:237], v[214:217], v[0:15]
	v_mfma_f32_32x32x16_bf16 v[16:31], v[234:237], v[218:221], v[16:31]
	s_cbranch_scc1 .LBB1_17
	s_mov_b32 s31, s28
	s_mov_b32 s33, s30
	s_branch .LBB1_8
